# P6 attention S^T: LDS K-fragment reads hoisted 5 deep (consumer order, address adds glued) + P7b fmac rewrite + P2 hoists + P1 tile permutation
# baseline (speedup 1.0000x reference)
.LBB0_648:
	s_ashr_i32 s12, s6, 6
	s_ashr_i32 s13, s12, 31
	s_lshl_b32 s10, s6, 7
	s_lshl_b32 s6, s6, 4
	s_and_b32 s35, s10, 0x780
	s_lshl_b64 s[10:11], s[12:13], 19
	s_and_b32 s6, s6, 0x300
	v_lshl_add_u64 v[2:3], v[98:99], 0, s[10:11]
	s_lshl_b32 s10, s6, 1
	s_mov_b32 s11, s7
	v_lshl_add_u64 v[2:3], v[2:3], 0, s[10:11]
	v_lshl_add_u64 v[62:63], v[2:3], 0, v[100:101]
	v_add_co_u32_e32 v6, vcc, s19, v62
	s_nop 1
	v_addc_co_u32_e32 v7, vcc, 0, v63, vcc
	v_add_co_u32_e32 v10, vcc, s17, v62
	s_barrier
	s_nop 0
	v_addc_co_u32_e32 v11, vcc, 0, v63, vcc
	v_add_co_u32_e32 v14, vcc, s18, v62
	s_nop 1
	v_addc_co_u32_e32 v15, vcc, 0, v63, vcc
	v_add_co_u32_e32 v18, vcc, s20, v62
	global_load_dwordx4 v[2:5], v[62:63], off
	s_nop 0
	v_addc_co_u32_e32 v19, vcc, 0, v63, vcc
	v_add_co_u32_e32 v22, vcc, s21, v62
	global_load_dwordx4 v[6:9], v[6:7], off
	s_nop 0
	v_addc_co_u32_e32 v23, vcc, 0, v63, vcc
	v_add_co_u32_e32 v26, vcc, s22, v62
	global_load_dwordx4 v[10:13], v[10:11], off
	s_nop 0
	v_addc_co_u32_e32 v27, vcc, 0, v63, vcc
	v_add_co_u32_e32 v30, vcc, s23, v62
	global_load_dwordx4 v[14:17], v[14:15], off
	s_nop 0
	v_addc_co_u32_e32 v31, vcc, 0, v63, vcc
	v_add_co_u32_e32 v34, vcc, s24, v62
	global_load_dwordx4 v[18:21], v[18:19], off
	s_nop 0
	v_addc_co_u32_e32 v35, vcc, 0, v63, vcc
	v_add_co_u32_e32 v38, vcc, s25, v62
	global_load_dwordx4 v[22:25], v[22:23], off
	s_nop 0
	v_addc_co_u32_e32 v39, vcc, 0, v63, vcc
	v_add_co_u32_e32 v42, vcc, s26, v62
	global_load_dwordx4 v[26:29], v[26:27], off
	s_nop 0
	v_addc_co_u32_e32 v43, vcc, 0, v63, vcc
	v_add_co_u32_e32 v46, vcc, s27, v62
	global_load_dwordx4 v[30:33], v[30:31], off
	s_nop 0
	v_addc_co_u32_e32 v47, vcc, 0, v63, vcc
	v_add_co_u32_e32 v50, vcc, s28, v62
	global_load_dwordx4 v[34:37], v[34:35], off
	s_nop 0
	v_addc_co_u32_e32 v51, vcc, 0, v63, vcc
	global_load_dwordx4 v[38:41], v[38:39], off
	v_add_co_u32_e32 v54, vcc, s29, v62
	global_load_dwordx4 v[42:45], v[42:43], off
	s_nop 0
	v_addc_co_u32_e32 v55, vcc, 0, v63, vcc
	global_load_dwordx4 v[46:49], v[46:47], off
	v_add_co_u32_e32 v58, vcc, s30, v62
	global_load_dwordx4 v[50:53], v[50:51], off
	s_nop 0
	v_addc_co_u32_e32 v59, vcc, 0, v63, vcc
	global_load_dwordx4 v[54:57], v[54:55], off
	v_add_co_u32_e32 v62, vcc, s31, v62
	global_load_dwordx4 v[58:61], v[58:59], off
	s_nop 0
	v_addc_co_u32_e32 v63, vcc, 0, v63, vcc
	global_load_dwordx4 v[62:65], v[62:63], off
	s_lshl_b64 s[36:37], s[12:13], 11
	s_add_u32 s13, s35, s15
	s_addc_u32 s35, 0, s16
	s_add_u32 s13, s13, s36
	v_add_u32_e32 v1, v95, v115
	s_addc_u32 s35, s35, s37
	v_mov_b32_e32 v103, v101
	v_add_u32_e32 v74, v116, v123
	v_add_u32_e32 v75, v116, v124
	s_lshl_b32 s12, s12, 8
	s_waitcnt vmcnt(15)
	ds_write_b128 v1, v[2:5]
	s_waitcnt vmcnt(14)
	ds_write_b128 v213, v[6:9]
	s_waitcnt vmcnt(13)
	ds_write_b128 v1, v[10:13] offset:16384
	s_waitcnt vmcnt(12)
	ds_write_b128 v214, v[14:17]
	s_waitcnt vmcnt(11)
	ds_write_b128 v1, v[18:21] offset:32768
	s_waitcnt vmcnt(10)
	ds_write_b128 v215, v[22:25]
	s_waitcnt vmcnt(9)
	ds_write_b128 v1, v[26:29] offset:49152
	s_waitcnt vmcnt(8)
	ds_write_b128 v216, v[30:33]
	s_waitcnt vmcnt(7)
	ds_write_b128 v217, v[34:37]
	s_waitcnt vmcnt(6)
	ds_write_b128 v218, v[38:41]
	s_waitcnt vmcnt(5)
	ds_write_b128 v219, v[42:45]
	s_waitcnt vmcnt(4)
	ds_write_b128 v220, v[46:49]
	s_waitcnt vmcnt(3)
	ds_write_b128 v221, v[50:53]
	s_waitcnt vmcnt(2)
	ds_write_b128 v222, v[54:57]
	s_waitcnt vmcnt(1)
	ds_write_b128 v223, v[58:61]
	s_waitcnt vmcnt(0)
	ds_write_b128 v224, v[62:65]
	v_mov_b32_e32 v3, s35
	v_or_b32_e32 v2, s13, v94
	v_lshlrev_b64 v[112:113], 11, v[2:3]
	v_lshl_add_u64 v[2:3], s[0:1], 0, v[112:113]
	v_lshl_add_u64 v[2:3], v[2:3], 0, s[10:11]
	v_lshl_add_u64 v[2:3], v[2:3], 0, v[102:103]
	global_load_dwordx4 v[70:73], v[2:3], off
	global_load_dwordx4 v[58:61], v[2:3], off offset:64
	global_load_dwordx4 v[46:49], v[2:3], off offset:128
	global_load_dwordx4 v[30:33], v[2:3], off offset:192
	global_load_dwordx4 v[26:29], v[2:3], off offset:256
	global_load_dwordx4 v[42:45], v[2:3], off offset:320
	global_load_dwordx4 v[66:69], v[2:3], off offset:384
	global_load_dwordx4 v[50:53], v[2:3], off offset:448
	v_add_u32_e32 v1, v116, v117
	s_waitcnt lgkmcnt(0)
	s_barrier
	ds_read_b128 v[232:235], v1
	v_add_u32_e32 v54, v116, v118
	ds_read_b128 v[236:239], v54
	v_add_u32_e32 v62, v116, v119
	ds_read_b128 v[240:243], v62
	v_add_u32_e32 v63, v116, v120
	ds_read_b128 v[244:247], v63
	v_add_u32_e32 v64, v116, v121
	ds_read_b128 v[248:251], v64
	v_add_u32_e32 v65, v116, v122
	s_ashr_i32 s13, s12, 31
	v_mov_b32_e32 v105, v101
	v_mov_b32_e32 v107, v101
	v_mov_b32_e32 v109, v101
	v_mov_b32_e32 v111, v101
	s_waitcnt vmcnt(7)
	s_waitcnt lgkmcnt(4)
	v_mfma_f32_16x16x32_bf16 v[2:5], v[232:235], v[70:73], 0
	ds_read_b128 v[232:235], v65
	s_add_i32 s33, s33, -1
	s_waitcnt vmcnt(6)
	s_waitcnt lgkmcnt(4)
	v_mfma_f32_16x16x32_bf16 v[2:5], v[236:239], v[58:61], v[2:5]
	ds_read_b128 v[236:239], v74
	s_waitcnt vmcnt(5)
	s_waitcnt lgkmcnt(4)
	v_mfma_f32_16x16x32_bf16 v[2:5], v[240:243], v[46:49], v[2:5]
	ds_read_b128 v[240:243], v75
	s_waitcnt vmcnt(4)
	s_waitcnt lgkmcnt(4)
	v_mfma_f32_16x16x32_bf16 v[2:5], v[244:247], v[30:33], v[2:5]
	ds_read_b128 v[244:247], v1 offset:2048
	s_waitcnt vmcnt(3)
	s_waitcnt lgkmcnt(4)
	v_mfma_f32_16x16x32_bf16 v[2:5], v[248:251], v[26:29], v[2:5]
	ds_read_b128 v[248:251], v54 offset:2048
	s_waitcnt vmcnt(2)
	s_waitcnt lgkmcnt(4)
	v_mfma_f32_16x16x32_bf16 v[2:5], v[232:235], v[42:45], v[2:5]
	ds_read_b128 v[232:235], v62 offset:2048
	s_waitcnt vmcnt(1)
	s_waitcnt lgkmcnt(4)
	v_mfma_f32_16x16x32_bf16 v[2:5], v[236:239], v[66:69], v[2:5]
	ds_read_b128 v[236:239], v63 offset:2048
	s_waitcnt vmcnt(0)
	s_waitcnt lgkmcnt(4)
	v_mfma_f32_16x16x32_bf16 v[2:5], v[240:243], v[50:53], v[2:5]
	ds_read_b128 v[240:243], v64 offset:2048
	s_nop 0
	s_waitcnt lgkmcnt(4)
	v_mfma_f32_16x16x32_bf16 v[6:9], v[244:247], v[70:73], 0
	ds_read_b128 v[244:247], v65 offset:2048
	s_waitcnt lgkmcnt(4)
	v_mfma_f32_16x16x32_bf16 v[6:9], v[248:251], v[58:61], v[6:9]
	ds_read_b128 v[248:251], v74 offset:2048
	s_nop 0
	s_waitcnt lgkmcnt(4)
	v_mfma_f32_16x16x32_bf16 v[6:9], v[232:235], v[46:49], v[6:9]
	ds_read_b128 v[232:235], v75 offset:2048
	s_nop 0
	s_waitcnt lgkmcnt(4)
	v_mfma_f32_16x16x32_bf16 v[6:9], v[236:239], v[30:33], v[6:9]
	ds_read_b128 v[236:239], v1 offset:16384
	s_nop 0
	s_waitcnt lgkmcnt(4)
	v_mfma_f32_16x16x32_bf16 v[6:9], v[240:243], v[26:29], v[6:9]
	ds_read_b128 v[240:243], v54 offset:16384
	s_nop 0
	s_waitcnt lgkmcnt(4)
	v_mfma_f32_16x16x32_bf16 v[6:9], v[244:247], v[42:45], v[6:9]
	ds_read_b128 v[244:247], v62 offset:16384
	s_nop 0
	s_waitcnt lgkmcnt(4)
	v_mfma_f32_16x16x32_bf16 v[6:9], v[248:251], v[66:69], v[6:9]
	ds_read_b128 v[248:251], v63 offset:16384
	s_nop 0
	s_waitcnt lgkmcnt(4)
	v_mfma_f32_16x16x32_bf16 v[18:21], v[232:235], v[50:53], v[6:9]
	ds_read_b128 v[232:235], v64 offset:16384
	s_nop 3
	s_nop 0
	s_waitcnt lgkmcnt(4)
	v_mfma_f32_16x16x32_bf16 v[6:9], v[236:239], v[70:73], 0
	ds_read_b128 v[236:239], v65 offset:16384
	s_nop 0
	s_waitcnt lgkmcnt(4)
	v_mfma_f32_16x16x32_bf16 v[6:9], v[240:243], v[58:61], v[6:9]
	ds_read_b128 v[240:243], v74 offset:16384
	s_nop 0
	s_waitcnt lgkmcnt(4)
	v_mfma_f32_16x16x32_bf16 v[6:9], v[244:247], v[46:49], v[6:9]
	ds_read_b128 v[244:247], v75 offset:16384
	s_nop 0
	s_waitcnt lgkmcnt(4)
	v_mfma_f32_16x16x32_bf16 v[6:9], v[248:251], v[30:33], v[6:9]
	ds_read_b128 v[248:251], v1 offset:18432
	s_nop 0
	s_waitcnt lgkmcnt(4)
	v_mfma_f32_16x16x32_bf16 v[6:9], v[232:235], v[26:29], v[6:9]
	ds_read_b128 v[232:235], v54 offset:18432
	s_nop 0
	s_waitcnt lgkmcnt(4)
	v_mfma_f32_16x16x32_bf16 v[6:9], v[236:239], v[42:45], v[6:9]
	ds_read_b128 v[236:239], v62 offset:18432
	s_nop 0
	s_waitcnt lgkmcnt(4)
	v_mfma_f32_16x16x32_bf16 v[6:9], v[240:243], v[66:69], v[6:9]
	ds_read_b128 v[240:243], v63 offset:18432
	s_nop 0
	s_waitcnt lgkmcnt(4)
	v_mfma_f32_16x16x32_bf16 v[6:9], v[244:247], v[50:53], v[6:9]
	ds_read_b128 v[244:247], v64 offset:18432
	s_nop 0
	s_waitcnt lgkmcnt(4)
	v_mfma_f32_16x16x32_bf16 v[10:13], v[248:251], v[70:73], 0
	ds_read_b128 v[248:251], v65 offset:18432
	s_waitcnt lgkmcnt(4)
	v_mfma_f32_16x16x32_bf16 v[10:13], v[232:235], v[58:61], v[10:13]
	ds_read_b128 v[232:235], v74 offset:18432
	s_nop 0
	s_waitcnt lgkmcnt(4)
	v_mfma_f32_16x16x32_bf16 v[10:13], v[236:239], v[46:49], v[10:13]
	ds_read_b128 v[236:239], v75 offset:18432
	s_nop 0
	s_waitcnt lgkmcnt(4)
	v_mfma_f32_16x16x32_bf16 v[10:13], v[240:243], v[30:33], v[10:13]
	ds_read_b128 v[240:243], v1 offset:32768
	s_nop 0
	s_waitcnt lgkmcnt(4)
	v_mfma_f32_16x16x32_bf16 v[10:13], v[244:247], v[26:29], v[10:13]
	ds_read_b128 v[244:247], v54 offset:32768
	s_nop 0
	s_waitcnt lgkmcnt(4)
	v_mfma_f32_16x16x32_bf16 v[10:13], v[248:251], v[42:45], v[10:13]
	ds_read_b128 v[248:251], v62 offset:32768
	s_nop 0
	s_waitcnt lgkmcnt(4)
	v_mfma_f32_16x16x32_bf16 v[10:13], v[232:235], v[66:69], v[10:13]
	ds_read_b128 v[232:235], v63 offset:32768
	s_nop 0
	s_waitcnt lgkmcnt(4)
	v_mfma_f32_16x16x32_bf16 v[22:25], v[236:239], v[50:53], v[10:13]
	ds_read_b128 v[236:239], v64 offset:32768
	s_nop 3
	s_nop 0
	s_waitcnt lgkmcnt(4)
	v_mfma_f32_16x16x32_bf16 v[10:13], v[240:243], v[70:73], 0
	ds_read_b128 v[240:243], v65 offset:32768
	s_nop 0
	s_waitcnt lgkmcnt(4)
	v_mfma_f32_16x16x32_bf16 v[10:13], v[244:247], v[58:61], v[10:13]
	ds_read_b128 v[244:247], v74 offset:32768
	s_nop 0
	s_waitcnt lgkmcnt(4)
	v_mfma_f32_16x16x32_bf16 v[10:13], v[248:251], v[46:49], v[10:13]
	ds_read_b128 v[248:251], v75 offset:32768
	s_nop 0
	s_waitcnt lgkmcnt(4)
	v_mfma_f32_16x16x32_bf16 v[10:13], v[232:235], v[30:33], v[10:13]
	ds_read_b128 v[232:235], v1 offset:34816
	s_nop 0
	s_waitcnt lgkmcnt(4)
	v_mfma_f32_16x16x32_bf16 v[10:13], v[236:239], v[26:29], v[10:13]
	ds_read_b128 v[236:239], v54 offset:34816
	s_nop 0
	s_waitcnt lgkmcnt(4)
	v_mfma_f32_16x16x32_bf16 v[10:13], v[240:243], v[42:45], v[10:13]
	ds_read_b128 v[240:243], v62 offset:34816
	s_nop 0
	s_waitcnt lgkmcnt(4)
	v_mfma_f32_16x16x32_bf16 v[10:13], v[244:247], v[66:69], v[10:13]
	ds_read_b128 v[244:247], v63 offset:34816
	s_nop 0
	s_waitcnt lgkmcnt(4)
	v_mfma_f32_16x16x32_bf16 v[10:13], v[248:251], v[50:53], v[10:13]
	ds_read_b128 v[248:251], v64 offset:34816
	s_nop 0
	s_waitcnt lgkmcnt(4)
	v_mfma_f32_16x16x32_bf16 v[14:17], v[232:235], v[70:73], 0
	ds_read_b128 v[232:235], v65 offset:34816
	s_waitcnt lgkmcnt(4)
	v_mfma_f32_16x16x32_bf16 v[14:17], v[236:239], v[58:61], v[14:17]
	ds_read_b128 v[236:239], v74 offset:34816
	s_nop 0
	s_waitcnt lgkmcnt(4)
	v_mfma_f32_16x16x32_bf16 v[14:17], v[240:243], v[46:49], v[14:17]
	ds_read_b128 v[240:243], v75 offset:34816
	s_nop 0
	s_waitcnt lgkmcnt(4)
	v_mfma_f32_16x16x32_bf16 v[14:17], v[244:247], v[30:33], v[14:17]
	ds_read_b128 v[244:247], v1 offset:49152
	s_nop 0
	s_waitcnt lgkmcnt(4)
	v_mfma_f32_16x16x32_bf16 v[14:17], v[248:251], v[26:29], v[14:17]
	ds_read_b128 v[248:251], v54 offset:49152
	s_nop 0
	s_waitcnt lgkmcnt(4)
	v_mfma_f32_16x16x32_bf16 v[14:17], v[232:235], v[42:45], v[14:17]
	ds_read_b128 v[232:235], v62 offset:49152
	s_nop 0
	s_waitcnt lgkmcnt(4)
	v_mfma_f32_16x16x32_bf16 v[14:17], v[236:239], v[66:69], v[14:17]
	ds_read_b128 v[236:239], v63 offset:49152
	s_nop 0
	s_waitcnt lgkmcnt(4)
	v_mfma_f32_16x16x32_bf16 v[34:37], v[240:243], v[50:53], v[14:17]
	ds_read_b128 v[240:243], v64 offset:49152
	s_nop 3
	s_nop 0
	s_waitcnt lgkmcnt(4)
	v_mfma_f32_16x16x32_bf16 v[14:17], v[244:247], v[70:73], 0
	ds_read_b128 v[244:247], v65 offset:49152
	s_waitcnt lgkmcnt(4)
	v_mfma_f32_16x16x32_bf16 v[14:17], v[248:251], v[58:61], v[14:17]
	ds_read_b128 v[248:251], v74 offset:49152
	s_nop 0
	s_waitcnt lgkmcnt(4)
	v_mfma_f32_16x16x32_bf16 v[14:17], v[232:235], v[46:49], v[14:17]
	ds_read_b128 v[232:235], v75 offset:49152
	s_nop 0
	s_waitcnt lgkmcnt(4)
	v_mfma_f32_16x16x32_bf16 v[14:17], v[236:239], v[30:33], v[14:17]
	ds_read_b128 v[236:239], v1 offset:51200
	s_nop 0
	s_waitcnt lgkmcnt(4)
	v_mfma_f32_16x16x32_bf16 v[14:17], v[240:243], v[26:29], v[14:17]
	ds_read_b128 v[240:243], v54 offset:51200
	s_nop 0
	s_waitcnt lgkmcnt(4)
	v_mfma_f32_16x16x32_bf16 v[14:17], v[244:247], v[42:45], v[14:17]
	ds_read_b128 v[244:247], v62 offset:51200
	s_nop 0
	s_waitcnt lgkmcnt(4)
	v_mfma_f32_16x16x32_bf16 v[14:17], v[248:251], v[66:69], v[14:17]
	ds_read_b128 v[248:251], v63 offset:51200
	s_nop 0
	s_waitcnt lgkmcnt(4)
	v_mfma_f32_16x16x32_bf16 v[14:17], v[232:235], v[50:53], v[14:17]
	ds_read_b128 v[232:235], v64 offset:51200
	s_nop 0
	s_waitcnt lgkmcnt(4)
	v_mfma_f32_16x16x32_bf16 v[38:41], v[236:239], v[70:73], 0
	ds_read_b128 v[236:239], v65 offset:51200
	s_waitcnt lgkmcnt(4)
	v_mfma_f32_16x16x32_bf16 v[38:41], v[240:243], v[58:61], v[38:41]
	ds_read_b128 v[240:243], v74 offset:51200
	s_nop 0
	s_waitcnt lgkmcnt(4)
	v_mfma_f32_16x16x32_bf16 v[38:41], v[244:247], v[46:49], v[38:41]
	ds_read_b128 v[244:247], v75 offset:51200
	s_nop 0
	s_waitcnt lgkmcnt(4)
	v_mfma_f32_16x16x32_bf16 v[38:41], v[248:251], v[30:33], v[38:41]
	v_add_u32_e32 v1, v125, v117
	ds_read_b128 v[248:251], v1
	s_nop 0
	s_waitcnt lgkmcnt(4)
	v_mfma_f32_16x16x32_bf16 v[38:41], v[232:235], v[26:29], v[38:41]
	v_add_u32_e32 v1, v125, v118
	ds_read_b128 v[232:235], v1
	s_nop 0
	s_waitcnt lgkmcnt(4)
	v_mfma_f32_16x16x32_bf16 v[38:41], v[236:239], v[42:45], v[38:41]
	v_add_u32_e32 v1, v125, v119
	ds_read_b128 v[236:239], v1
	s_nop 0
	s_waitcnt lgkmcnt(4)
	v_mfma_f32_16x16x32_bf16 v[38:41], v[240:243], v[66:69], v[38:41]
	v_add_u32_e32 v1, v125, v120
	ds_read_b128 v[240:243], v1
	s_nop 0
	s_waitcnt lgkmcnt(4)
	v_mfma_f32_16x16x32_bf16 v[38:41], v[244:247], v[50:53], v[38:41]
	v_add_u32_e32 v1, v125, v121
	ds_read_b128 v[244:247], v1
	s_nop 0
	s_waitcnt lgkmcnt(4)
	v_mfma_f32_16x16x32_bf16 v[54:57], v[248:251], v[70:73], 0
	v_add_u32_e32 v1, v125, v122
	ds_read_b128 v[248:251], v1
	s_nop 0
	s_waitcnt lgkmcnt(4)
	v_mfma_f32_16x16x32_bf16 v[54:57], v[232:235], v[58:61], v[54:57]
	v_add_u32_e32 v1, v125, v123
	ds_read_b128 v[232:235], v1
	s_nop 0
	s_waitcnt lgkmcnt(4)
	v_mfma_f32_16x16x32_bf16 v[54:57], v[236:239], v[46:49], v[54:57]
	v_add_u32_e32 v1, v125, v124
	ds_read_b128 v[236:239], v1
	s_nop 0
	s_waitcnt lgkmcnt(4)
	v_mfma_f32_16x16x32_bf16 v[54:57], v[240:243], v[30:33], v[54:57]
	v_add_u32_e32 v1, v126, v117
	ds_read_b128 v[240:243], v1
	s_nop 0
	s_waitcnt lgkmcnt(4)
	v_mfma_f32_16x16x32_bf16 v[54:57], v[244:247], v[26:29], v[54:57]
	v_add_u32_e32 v1, v126, v118
	ds_read_b128 v[244:247], v1
	s_nop 0
	s_waitcnt lgkmcnt(4)
	v_mfma_f32_16x16x32_bf16 v[54:57], v[248:251], v[42:45], v[54:57]
	v_add_u32_e32 v1, v126, v119
	ds_read_b128 v[248:251], v1
	s_nop 0
	s_waitcnt lgkmcnt(4)
	v_mfma_f32_16x16x32_bf16 v[54:57], v[232:235], v[66:69], v[54:57]
	v_add_u32_e32 v1, v126, v120
	ds_read_b128 v[232:235], v1
	s_nop 0
	s_waitcnt lgkmcnt(4)
	v_mfma_f32_16x16x32_bf16 v[54:57], v[236:239], v[50:53], v[54:57]
	v_add_u32_e32 v1, v126, v121
	ds_read_b128 v[236:239], v1
	s_nop 0
	s_waitcnt lgkmcnt(4)
	v_mfma_f32_16x16x32_bf16 v[62:65], v[240:243], v[70:73], 0
	v_add_u32_e32 v1, v126, v122
	ds_read_b128 v[240:243], v1
	s_nop 0
	s_waitcnt lgkmcnt(4)
	v_mfma_f32_16x16x32_bf16 v[62:65], v[244:247], v[58:61], v[62:65]
	v_add_u32_e32 v1, v126, v123
	ds_read_b128 v[244:247], v1
	s_nop 0
	s_waitcnt lgkmcnt(4)
	v_mfma_f32_16x16x32_bf16 v[62:65], v[248:251], v[46:49], v[62:65]
	v_add_u32_e32 v1, v126, v124
	ds_read_b128 v[248:251], v1
	s_nop 0
	s_waitcnt lgkmcnt(4)
	v_mfma_f32_16x16x32_bf16 v[62:65], v[232:235], v[30:33], v[62:65]
	v_add_u32_e32 v1, v127, v117
	ds_read_b128 v[232:235], v1
	s_nop 0
	s_waitcnt lgkmcnt(4)
	v_mfma_f32_16x16x32_bf16 v[62:65], v[236:239], v[26:29], v[62:65]
	v_add_u32_e32 v1, v127, v118
	ds_read_b128 v[236:239], v1
	s_nop 0
	s_waitcnt lgkmcnt(4)
	v_mfma_f32_16x16x32_bf16 v[62:65], v[240:243], v[42:45], v[62:65]
	v_add_u32_e32 v1, v127, v119
	ds_read_b128 v[240:243], v1
	s_nop 0
	s_waitcnt lgkmcnt(4)
	v_mfma_f32_16x16x32_bf16 v[62:65], v[244:247], v[66:69], v[62:65]
	v_add_u32_e32 v1, v127, v120
	ds_read_b128 v[244:247], v1
	s_nop 0
	s_waitcnt lgkmcnt(4)
	v_mfma_f32_16x16x32_bf16 v[62:65], v[248:251], v[50:53], v[62:65]
	v_add_u32_e32 v1, v127, v121
	ds_read_b128 v[248:251], v1
	s_nop 0
	s_waitcnt lgkmcnt(4)
	v_mfma_f32_16x16x32_bf16 v[74:77], v[232:235], v[70:73], 0
	v_add_u32_e32 v1, v127, v122
	ds_read_b128 v[232:235], v1
	s_nop 0
	s_waitcnt lgkmcnt(4)
	v_mfma_f32_16x16x32_bf16 v[74:77], v[236:239], v[58:61], v[74:77]
	v_add_u32_e32 v1, v127, v123
	ds_read_b128 v[236:239], v1
	s_nop 0
	s_waitcnt lgkmcnt(4)
	v_mfma_f32_16x16x32_bf16 v[74:77], v[240:243], v[46:49], v[74:77]
	v_add_u32_e32 v1, v127, v124
	ds_read_b128 v[240:243], v1
	s_nop 0
	s_waitcnt lgkmcnt(4)
	v_mfma_f32_16x16x32_bf16 v[74:77], v[244:247], v[30:33], v[74:77]
	v_add_u32_e32 v1, v128, v117
	ds_read_b128 v[244:247], v1
	s_nop 0
	s_waitcnt lgkmcnt(4)
	v_mfma_f32_16x16x32_bf16 v[74:77], v[248:251], v[26:29], v[74:77]
	v_add_u32_e32 v1, v128, v118
	ds_read_b128 v[248:251], v1
	s_nop 0
	s_waitcnt lgkmcnt(4)
	v_mfma_f32_16x16x32_bf16 v[74:77], v[232:235], v[42:45], v[74:77]
	v_add_u32_e32 v1, v128, v119
	ds_read_b128 v[232:235], v1
	s_nop 0
	s_waitcnt lgkmcnt(4)
	v_mfma_f32_16x16x32_bf16 v[74:77], v[236:239], v[66:69], v[74:77]
	v_add_u32_e32 v1, v128, v120
	ds_read_b128 v[236:239], v1
	s_nop 0
	s_waitcnt lgkmcnt(4)
	v_mfma_f32_16x16x32_bf16 v[74:77], v[240:243], v[50:53], v[74:77]
	v_add_u32_e32 v1, v128, v121
	ds_read_b128 v[240:243], v1
	s_nop 0
	s_waitcnt lgkmcnt(4)
	v_mfma_f32_16x16x32_bf16 v[78:81], v[244:247], v[70:73], 0
	v_add_u32_e32 v1, v128, v122
	ds_read_b128 v[244:247], v1
	s_nop 0
	s_waitcnt lgkmcnt(4)
	v_mfma_f32_16x16x32_bf16 v[78:81], v[248:251], v[58:61], v[78:81]
	v_add_u32_e32 v1, v128, v123
	ds_read_b128 v[248:251], v1
	s_nop 0
	s_waitcnt lgkmcnt(4)
	v_mfma_f32_16x16x32_bf16 v[78:81], v[232:235], v[46:49], v[78:81]
	v_add_u32_e32 v1, v128, v124
	ds_read_b128 v[232:235], v1
	s_nop 0
	s_waitcnt lgkmcnt(4)
	v_mfma_f32_16x16x32_bf16 v[78:81], v[236:239], v[30:33], v[78:81]
	v_add_u32_e32 v1, v129, v117
	ds_read_b128 v[236:239], v1
	s_nop 0
	s_waitcnt lgkmcnt(4)
	v_mfma_f32_16x16x32_bf16 v[78:81], v[240:243], v[26:29], v[78:81]
	v_add_u32_e32 v1, v129, v118
	ds_read_b128 v[240:243], v1
	s_nop 0
	s_waitcnt lgkmcnt(4)
	v_mfma_f32_16x16x32_bf16 v[78:81], v[244:247], v[42:45], v[78:81]
	v_add_u32_e32 v1, v129, v119
	ds_read_b128 v[244:247], v1
	s_nop 0
	s_waitcnt lgkmcnt(4)
	v_mfma_f32_16x16x32_bf16 v[78:81], v[248:251], v[66:69], v[78:81]
	v_add_u32_e32 v1, v129, v120
	ds_read_b128 v[248:251], v1
	s_nop 0
	s_waitcnt lgkmcnt(4)
	v_mfma_f32_16x16x32_bf16 v[78:81], v[232:235], v[50:53], v[78:81]
	v_add_u32_e32 v1, v129, v121
	ds_read_b128 v[232:235], v1
	s_nop 0
	s_waitcnt lgkmcnt(4)
	v_mfma_f32_16x16x32_bf16 v[82:85], v[236:239], v[70:73], 0
	v_add_u32_e32 v1, v129, v122
	ds_read_b128 v[236:239], v1
	s_nop 0
	s_waitcnt lgkmcnt(4)
	v_mfma_f32_16x16x32_bf16 v[82:85], v[240:243], v[58:61], v[82:85]
	v_add_u32_e32 v1, v129, v123
	ds_read_b128 v[240:243], v1
	s_nop 0
	s_waitcnt lgkmcnt(4)
	v_mfma_f32_16x16x32_bf16 v[82:85], v[244:247], v[46:49], v[82:85]
	v_add_u32_e32 v1, v129, v124
	ds_read_b128 v[244:247], v1
	s_nop 0
	s_waitcnt lgkmcnt(4)
	v_mfma_f32_16x16x32_bf16 v[82:85], v[248:251], v[30:33], v[82:85]
	v_add_u32_e32 v1, v130, v117
	ds_read_b128 v[248:251], v1
	s_nop 0
	s_waitcnt lgkmcnt(4)
	v_mfma_f32_16x16x32_bf16 v[82:85], v[232:235], v[26:29], v[82:85]
	v_add_u32_e32 v1, v130, v118
	ds_read_b128 v[232:235], v1
	s_nop 0
	s_waitcnt lgkmcnt(4)
	v_mfma_f32_16x16x32_bf16 v[82:85], v[236:239], v[42:45], v[82:85]
	v_add_u32_e32 v1, v130, v119
	ds_read_b128 v[236:239], v1
	s_nop 0
	s_waitcnt lgkmcnt(4)
	v_mfma_f32_16x16x32_bf16 v[82:85], v[240:243], v[66:69], v[82:85]
	v_add_u32_e32 v1, v130, v120
	ds_read_b128 v[240:243], v1
	s_nop 0
	s_waitcnt lgkmcnt(4)
	v_mfma_f32_16x16x32_bf16 v[82:85], v[244:247], v[50:53], v[82:85]
	v_add_u32_e32 v1, v130, v121
	ds_read_b128 v[244:247], v1
	s_nop 0
	s_waitcnt lgkmcnt(4)
	v_mfma_f32_16x16x32_bf16 v[86:89], v[248:251], v[70:73], 0
	v_add_u32_e32 v1, v130, v122
	ds_read_b128 v[248:251], v1
	s_nop 0
	s_waitcnt lgkmcnt(4)
	v_mfma_f32_16x16x32_bf16 v[86:89], v[232:235], v[58:61], v[86:89]
	v_add_u32_e32 v1, v130, v123
	ds_read_b128 v[232:235], v1
	s_nop 0
	s_waitcnt lgkmcnt(4)
	v_mfma_f32_16x16x32_bf16 v[86:89], v[236:239], v[46:49], v[86:89]
	v_add_u32_e32 v1, v130, v124
	ds_read_b128 v[236:239], v1
	s_nop 0
	s_waitcnt lgkmcnt(4)
	v_mfma_f32_16x16x32_bf16 v[86:89], v[240:243], v[30:33], v[86:89]
	v_add_u32_e32 v1, v131, v117
	ds_read_b128 v[240:243], v1
	s_nop 0
	s_waitcnt lgkmcnt(4)
	v_mfma_f32_16x16x32_bf16 v[86:89], v[244:247], v[26:29], v[86:89]
	v_add_u32_e32 v1, v131, v118
	ds_read_b128 v[244:247], v1
	s_nop 0
	s_waitcnt lgkmcnt(4)
	v_mfma_f32_16x16x32_bf16 v[86:89], v[248:251], v[42:45], v[86:89]
	v_add_u32_e32 v1, v131, v119
	ds_read_b128 v[248:251], v1
	s_nop 0
	s_waitcnt lgkmcnt(4)
	v_mfma_f32_16x16x32_bf16 v[86:89], v[232:235], v[66:69], v[86:89]
	v_add_u32_e32 v1, v131, v120
	ds_read_b128 v[232:235], v1
	s_nop 0
	s_waitcnt lgkmcnt(4)
	v_mfma_f32_16x16x32_bf16 v[86:89], v[236:239], v[50:53], v[86:89]
	v_add_u32_e32 v1, v131, v121
	ds_read_b128 v[236:239], v1
	s_nop 0
	s_waitcnt lgkmcnt(4)
	v_mfma_f32_16x16x32_bf16 v[90:93], v[240:243], v[70:73], 0
	v_add_u32_e32 v1, v131, v122
	ds_read_b128 v[240:243], v1
	s_nop 0
	s_waitcnt lgkmcnt(4)
	v_mfma_f32_16x16x32_bf16 v[90:93], v[244:247], v[58:61], v[90:93]
	v_add_u32_e32 v1, v131, v123
	ds_read_b128 v[244:247], v1
	s_nop 0
	s_waitcnt lgkmcnt(4)
	v_mfma_f32_16x16x32_bf16 v[90:93], v[248:251], v[46:49], v[90:93]
	v_add_u32_e32 v1, v131, v124
	ds_read_b128 v[248:251], v1
	s_nop 0
	s_waitcnt lgkmcnt(4)
	v_mfma_f32_16x16x32_bf16 v[90:93], v[232:235], v[30:33], v[90:93]
	v_add_u32_e32 v1, v132, v117
	ds_read_b128 v[232:235], v1
	s_nop 0
	s_waitcnt lgkmcnt(4)
	v_mfma_f32_16x16x32_bf16 v[90:93], v[236:239], v[26:29], v[90:93]
	v_add_u32_e32 v1, v132, v118
	ds_read_b128 v[236:239], v1
	s_nop 0
	s_waitcnt lgkmcnt(4)
	v_mfma_f32_16x16x32_bf16 v[90:93], v[240:243], v[42:45], v[90:93]
	v_add_u32_e32 v1, v132, v119
	ds_read_b128 v[240:243], v1
	s_nop 0
	s_waitcnt lgkmcnt(4)
	v_mfma_f32_16x16x32_bf16 v[90:93], v[244:247], v[66:69], v[90:93]
	v_add_u32_e32 v1, v132, v120
	ds_read_b128 v[244:247], v1
	s_nop 0
	s_waitcnt lgkmcnt(4)
	v_mfma_f32_16x16x32_bf16 v[90:93], v[248:251], v[50:53], v[90:93]
	v_add_u32_e32 v1, v132, v121
	ds_read_b128 v[248:251], v1
	s_nop 0
	s_waitcnt lgkmcnt(4)
	v_mfma_f32_16x16x32_bf16 v[70:73], v[232:235], v[70:73], 0
	v_add_u32_e32 v1, v132, v122
	ds_read_b128 v[232:235], v1
	s_nop 0
	s_waitcnt lgkmcnt(4)
	v_mfma_f32_16x16x32_bf16 v[58:61], v[236:239], v[58:61], v[70:73]
	v_add_u32_e32 v1, v132, v123
	ds_read_b128 v[236:239], v1
	s_nop 3
	s_nop 0
	s_waitcnt lgkmcnt(4)
	v_mfma_f32_16x16x32_bf16 v[46:49], v[240:243], v[46:49], v[58:61]
	s_nop 2
	s_nop 0
	s_waitcnt lgkmcnt(3)
	v_mfma_f32_16x16x32_bf16 v[30:33], v[244:247], v[30:33], v[46:49]
	s_nop 2
	s_nop 0
	s_waitcnt lgkmcnt(2)
	v_mfma_f32_16x16x32_bf16 v[26:29], v[248:251], v[26:29], v[30:33]
	s_nop 2
	s_nop 0
	s_waitcnt lgkmcnt(1)
	v_mfma_f32_16x16x32_bf16 v[26:29], v[232:235], v[42:45], v[26:29]
	s_nop 0
	s_waitcnt lgkmcnt(0)
	v_mfma_f32_16x16x32_bf16 v[26:29], v[236:239], v[66:69], v[26:29]
	v_add_u32_e32 v1, v132, v124
	ds_read_b128 v[30:33], v1
	v_max3_f32 v1, v2, v3, v4
	v_max3_f32 v1, v1, v5, v18
	s_waitcnt lgkmcnt(0)
	v_mfma_f32_16x16x32_bf16 v[26:29], v[30:33], v[50:53], v[26:29]
	v_max_f32_e32 v30, v20, v20
	v_max_f32_e32 v31, v19, v19
	v_max_f32_e32 v30, v31, v30
	v_max3_f32 v1, v1, v30, v21
	v_max_f32_e32 v30, v8, v8
	v_max_f32_e32 v31, v7, v7
	v_max_f32_e32 v30, v31, v30
	v_max3_f32 v1, v1, v6, v30
	v_max_f32_e32 v30, v24, v24
	v_max_f32_e32 v31, v23, v23
	v_max3_f32 v1, v1, v9, v22
	v_max_f32_e32 v30, v31, v30
	v_max3_f32 v1, v1, v30, v25
	v_max_f32_e32 v30, v12, v12
	v_max_f32_e32 v31, v11, v11
	v_max_f32_e32 v30, v31, v30
	v_max3_f32 v1, v1, v10, v30
	v_max_f32_e32 v30, v36, v36
	v_max_f32_e32 v31, v35, v35
	v_max3_f32 v1, v1, v13, v34
	v_max_f32_e32 v30, v31, v30
	v_max3_f32 v1, v1, v30, v37
	v_max_f32_e32 v30, v16, v16
	v_max_f32_e32 v31, v15, v15
	v_max_f32_e32 v30, v31, v30
	v_max3_f32 v1, v1, v14, v30
	v_max_f32_e32 v30, v40, v40
	v_max_f32_e32 v31, v39, v39
	v_max3_f32 v1, v1, v17, v38
	v_max_f32_e32 v30, v31, v30
	v_max3_f32 v1, v1, v30, v41
	v_max_f32_e32 v30, v56, v56
	v_max_f32_e32 v31, v55, v55
	v_max_f32_e32 v30, v31, v30
	v_max3_f32 v1, v1, v54, v30
	v_max_f32_e32 v30, v64, v64
	v_max_f32_e32 v31, v63, v63
	v_max3_f32 v1, v1, v57, v62
	v_max_f32_e32 v30, v31, v30
	v_max3_f32 v1, v1, v30, v65
	v_max_f32_e32 v30, v76, v76
	v_max_f32_e32 v31, v75, v75
	v_max_f32_e32 v30, v31, v30
	v_max3_f32 v1, v1, v74, v30
	v_max_f32_e32 v30, v80, v80
	v_max_f32_e32 v31, v79, v79
	v_max3_f32 v1, v1, v77, v78
	v_max_f32_e32 v30, v31, v30
	v_max3_f32 v1, v1, v30, v81
	v_max_f32_e32 v30, v84, v84
	v_max_f32_e32 v31, v83, v83
	v_max_f32_e32 v30, v31, v30
	v_max3_f32 v1, v1, v82, v30
	v_max_f32_e32 v30, v88, v88
	v_max_f32_e32 v31, v87, v87
	v_max3_f32 v1, v1, v85, v86
	v_max_f32_e32 v30, v31, v30
	v_max3_f32 v1, v1, v30, v89
	v_max_f32_e32 v30, v92, v92
	v_max_f32_e32 v31, v91, v91
	v_max_f32_e32 v30, v31, v30
	v_max3_f32 v1, v1, v90, v30
	v_max_f32_e32 v30, v28, v28
	v_max_f32_e32 v31, v27, v27
	v_max3_f32 v1, v1, v93, v26
	v_max_f32_e32 v30, v31, v30
	v_and_b32_e32 v31, 64, v230
	v_max3_f32 v30, v1, v30, v29
	v_xor_b32_e32 v1, 16, v230
	v_add_u32_e32 v31, 64, v31
	v_cmp_lt_i32_e32 vcc, v1, v31
	s_nop 1
	v_cndmask_b32_e32 v1, v230, v1, vcc
	v_lshlrev_b32_e32 v1, 2, v1
	ds_bpermute_b32 v32, v1, v30
	s_waitcnt lgkmcnt(0)
	v_max_f32_e32 v32, v32, v32
	v_max_f32_e32 v32, v30, v32
	v_xor_b32_e32 v30, 32, v230
	v_cmp_lt_i32_e32 vcc, v30, v31
	s_nop 1
	v_cndmask_b32_e32 v30, v230, v30, vcc
	v_lshlrev_b32_e32 v30, 2, v30
	ds_bpermute_b32 v31, v30, v32
	s_waitcnt lgkmcnt(0)
	v_max_f32_e32 v31, v31, v31
	v_max_f32_e32 v31, v32, v31
	v_sub_f32_e32 v33, v34, v31
	v_mul_f32_e32 v33, 0x3db8aa3b, v33
	v_exp_f32_e32 v34, v33
	v_sub_f32_e32 v33, v35, v31
	v_mul_f32_e32 v33, 0x3db8aa3b, v33
	v_exp_f32_e32 v35, v33
	v_sub_f32_e32 v33, v36, v31
	v_mul_f32_e32 v33, 0x3db8aa3b, v33
	v_exp_f32_e32 v36, v33
	v_sub_f32_e32 v33, v37, v31
	v_mul_f32_e32 v33, 0x3db8aa3b, v33
	v_exp_f32_e32 v37, v33
	v_sub_f32_e32 v33, v38, v31
	v_mul_f32_e32 v33, 0x3db8aa3b, v33
	v_exp_f32_e32 v38, v33
	v_sub_f32_e32 v33, v39, v31
	v_sub_f32_e32 v2, v2, v31
	v_mul_f32_e32 v33, 0x3db8aa3b, v33
	v_mul_f32_e32 v2, 0x3db8aa3b, v2
	v_sub_f32_e32 v3, v3, v31
	v_exp_f32_e32 v39, v33
	v_sub_f32_e32 v33, v40, v31
	v_exp_f32_e32 v2, v2
	v_mul_f32_e32 v3, 0x3db8aa3b, v3
	v_sub_f32_e32 v4, v4, v31
	v_mul_f32_e32 v33, 0x3db8aa3b, v33
	v_exp_f32_e32 v3, v3
	v_mul_f32_e32 v4, 0x3db8aa3b, v4
	v_sub_f32_e32 v5, v5, v31
	v_exp_f32_e32 v40, v33
	v_sub_f32_e32 v33, v41, v31
	v_exp_f32_e32 v4, v4
	v_mul_f32_e32 v5, 0x3db8aa3b, v5
	v_sub_f32_e32 v18, v18, v31
	v_mul_f32_e32 v33, 0x3db8aa3b, v33
	v_exp_f32_e32 v5, v5
	v_mul_f32_e32 v18, 0x3db8aa3b, v18
	v_sub_f32_e32 v19, v19, v31
	v_exp_f32_e32 v41, v33
	v_sub_f32_e32 v33, v54, v31
	v_add_f32_e32 v32, 0, v2
	v_exp_f32_e32 v18, v18
	v_mul_f32_e32 v19, 0x3db8aa3b, v19
	v_sub_f32_e32 v20, v20, v31
	v_mul_f32_e32 v33, 0x3db8aa3b, v33
	v_add_f32_e32 v32, v32, v3
	v_exp_f32_e32 v19, v19
	v_mul_f32_e32 v20, 0x3db8aa3b, v20
	v_sub_f32_e32 v21, v21, v31
	v_exp_f32_e32 v42, v33
	v_sub_f32_e32 v33, v55, v31
	v_add_f32_e32 v32, v32, v4
	v_exp_f32_e32 v20, v20
	v_mul_f32_e32 v21, 0x3db8aa3b, v21
	v_sub_f32_e32 v6, v6, v31
	v_mul_f32_e32 v33, 0x3db8aa3b, v33
	v_add_f32_e32 v32, v32, v5
	v_exp_f32_e32 v21, v21
	v_mul_f32_e32 v6, 0x3db8aa3b, v6
	v_sub_f32_e32 v7, v7, v31
	v_exp_f32_e32 v43, v33
	v_sub_f32_e32 v33, v56, v31
	v_add_f32_e32 v32, v32, v18
	v_exp_f32_e32 v6, v6
	v_mul_f32_e32 v7, 0x3db8aa3b, v7
	v_sub_f32_e32 v8, v8, v31
	v_mul_f32_e32 v33, 0x3db8aa3b, v33
	v_add_f32_e32 v32, v32, v19
	v_exp_f32_e32 v7, v7
	v_mul_f32_e32 v8, 0x3db8aa3b, v8
	v_sub_f32_e32 v9, v9, v31
	v_exp_f32_e32 v44, v33
	v_sub_f32_e32 v33, v57, v31
	v_add_f32_e32 v32, v32, v20
	v_exp_f32_e32 v8, v8
	v_mul_f32_e32 v9, 0x3db8aa3b, v9
	v_sub_f32_e32 v22, v22, v31
	v_mul_f32_e32 v33, 0x3db8aa3b, v33
	v_add_f32_e32 v32, v32, v21
	v_exp_f32_e32 v9, v9
	v_mul_f32_e32 v22, 0x3db8aa3b, v22
	v_sub_f32_e32 v23, v23, v31
	v_exp_f32_e32 v45, v33
	v_sub_f32_e32 v33, v62, v31
	v_add_f32_e32 v32, v32, v6
	v_exp_f32_e32 v22, v22
	v_mul_f32_e32 v23, 0x3db8aa3b, v23
	v_sub_f32_e32 v24, v24, v31
	v_mul_f32_e32 v33, 0x3db8aa3b, v33
	v_add_f32_e32 v32, v32, v7
	v_exp_f32_e32 v23, v23
	v_mul_f32_e32 v24, 0x3db8aa3b, v24
	v_sub_f32_e32 v25, v25, v31
	v_exp_f32_e32 v46, v33
	v_sub_f32_e32 v33, v63, v31
	v_add_f32_e32 v32, v32, v8
	v_exp_f32_e32 v24, v24
	v_mul_f32_e32 v25, 0x3db8aa3b, v25
	v_sub_f32_e32 v10, v10, v31
	v_mul_f32_e32 v33, 0x3db8aa3b, v33
	v_add_f32_e32 v32, v32, v9
	v_exp_f32_e32 v25, v25
	v_mul_f32_e32 v10, 0x3db8aa3b, v10
	v_sub_f32_e32 v11, v11, v31
	v_exp_f32_e32 v47, v33
	v_sub_f32_e32 v33, v64, v31
	v_add_f32_e32 v32, v32, v22
	v_exp_f32_e32 v10, v10
	v_mul_f32_e32 v11, 0x3db8aa3b, v11
	v_sub_f32_e32 v12, v12, v31
	v_mul_f32_e32 v33, 0x3db8aa3b, v33
	v_add_f32_e32 v32, v32, v23
	v_exp_f32_e32 v11, v11
	v_mul_f32_e32 v12, 0x3db8aa3b, v12
	v_sub_f32_e32 v13, v13, v31
	v_exp_f32_e32 v48, v33
	v_sub_f32_e32 v33, v65, v31
	v_add_f32_e32 v32, v32, v24
	v_exp_f32_e32 v12, v12
	v_mul_f32_e32 v13, 0x3db8aa3b, v13
	v_mul_f32_e32 v33, 0x3db8aa3b, v33
	v_add_f32_e32 v32, v32, v25
	v_exp_f32_e32 v13, v13
	v_exp_f32_e32 v49, v33
	v_sub_f32_e32 v33, v74, v31
	v_add_f32_e32 v32, v32, v10
	v_mul_f32_e32 v33, 0x3db8aa3b, v33
	v_add_f32_e32 v32, v32, v11
	v_exp_f32_e32 v50, v33
	v_sub_f32_e32 v33, v75, v31
	v_add_f32_e32 v32, v32, v12
	v_sub_f32_e32 v14, v14, v31
	v_mul_f32_e32 v33, 0x3db8aa3b, v33
	v_add_f32_e32 v32, v32, v13
	v_mul_f32_e32 v14, 0x3db8aa3b, v14
	v_sub_f32_e32 v15, v15, v31
	v_exp_f32_e32 v51, v33
	v_sub_f32_e32 v33, v76, v31
	v_add_f32_e32 v32, v32, v34
	v_exp_f32_e32 v14, v14
	v_mul_f32_e32 v15, 0x3db8aa3b, v15
	v_sub_f32_e32 v16, v16, v31
	v_mul_f32_e32 v33, 0x3db8aa3b, v33
	v_add_f32_e32 v32, v32, v35
	v_exp_f32_e32 v15, v15
	v_mul_f32_e32 v16, 0x3db8aa3b, v16
	v_sub_f32_e32 v17, v17, v31
	v_exp_f32_e32 v52, v33
	v_sub_f32_e32 v33, v77, v31
	v_add_f32_e32 v32, v32, v36
	v_exp_f32_e32 v16, v16
	v_mul_f32_e32 v17, 0x3db8aa3b, v17
	v_mul_f32_e32 v33, 0x3db8aa3b, v33
	v_add_f32_e32 v32, v32, v37
	v_exp_f32_e32 v17, v17
	v_exp_f32_e32 v53, v33
	v_sub_f32_e32 v33, v78, v31
	v_add_f32_e32 v32, v32, v14
	v_mul_f32_e32 v33, 0x3db8aa3b, v33
	v_add_f32_e32 v32, v32, v15
	v_exp_f32_e32 v54, v33
	v_sub_f32_e32 v33, v79, v31
	v_add_f32_e32 v32, v32, v16
	v_mul_f32_e32 v33, 0x3db8aa3b, v33
	v_add_f32_e32 v32, v32, v17
	v_exp_f32_e32 v55, v33
	v_sub_f32_e32 v33, v80, v31
	v_add_f32_e32 v32, v32, v38
	v_mul_f32_e32 v33, 0x3db8aa3b, v33
	v_add_f32_e32 v32, v32, v39
	v_exp_f32_e32 v56, v33
	v_sub_f32_e32 v33, v81, v31
	v_add_f32_e32 v32, v32, v40
	v_mul_f32_e32 v33, 0x3db8aa3b, v33
	v_add_f32_e32 v32, v32, v41
	v_exp_f32_e32 v57, v33
	v_sub_f32_e32 v33, v82, v31
	v_add_f32_e32 v32, v32, v42
	v_mul_f32_e32 v33, 0x3db8aa3b, v33
	v_add_f32_e32 v32, v32, v43
	v_exp_f32_e32 v58, v33
	v_sub_f32_e32 v33, v83, v31
	v_add_f32_e32 v32, v32, v44
	v_mul_f32_e32 v33, 0x3db8aa3b, v33
	v_add_f32_e32 v32, v32, v45
	v_exp_f32_e32 v59, v33
	v_sub_f32_e32 v33, v84, v31
	v_add_f32_e32 v32, v32, v46
	v_mul_f32_e32 v33, 0x3db8aa3b, v33
	v_add_f32_e32 v32, v32, v47
	v_exp_f32_e32 v60, v33
	v_sub_f32_e32 v33, v85, v31
	v_add_f32_e32 v32, v32, v48
	v_mul_f32_e32 v33, 0x3db8aa3b, v33
	v_add_f32_e32 v32, v32, v49
	v_exp_f32_e32 v61, v33
	v_sub_f32_e32 v33, v86, v31
	v_add_f32_e32 v32, v32, v50
	v_mul_f32_e32 v33, 0x3db8aa3b, v33
	v_add_f32_e32 v32, v32, v51
	v_exp_f32_e32 v62, v33
	v_sub_f32_e32 v33, v87, v31
	v_add_f32_e32 v32, v32, v52
	v_mul_f32_e32 v33, 0x3db8aa3b, v33
	v_add_f32_e32 v32, v32, v53
	v_exp_f32_e32 v63, v33
	v_sub_f32_e32 v33, v88, v31
	v_add_f32_e32 v32, v32, v54
	v_mul_f32_e32 v33, 0x3db8aa3b, v33
	v_add_f32_e32 v32, v32, v55
	v_exp_f32_e32 v64, v33
	v_sub_f32_e32 v33, v89, v31
	v_add_f32_e32 v32, v32, v56
	v_mul_f32_e32 v33, 0x3db8aa3b, v33
	v_add_f32_e32 v32, v32, v57
	v_exp_f32_e32 v65, v33
	v_sub_f32_e32 v33, v90, v31
	v_add_f32_e32 v32, v32, v58
	v_mul_f32_e32 v33, 0x3db8aa3b, v33
	v_add_f32_e32 v32, v32, v59
	v_exp_f32_e32 v66, v33
	v_sub_f32_e32 v33, v91, v31
	v_add_f32_e32 v32, v32, v60
	v_mul_f32_e32 v33, 0x3db8aa3b, v33
	v_add_f32_e32 v32, v32, v61
	v_exp_f32_e32 v67, v33
	v_sub_f32_e32 v33, v92, v31
	v_add_f32_e32 v32, v32, v62
	v_mul_f32_e32 v33, 0x3db8aa3b, v33
	v_add_f32_e32 v32, v32, v63
	v_exp_f32_e32 v68, v33
	v_sub_f32_e32 v33, v93, v31
	v_sub_f32_e32 v27, v27, v31
	v_add_f32_e32 v32, v32, v64
	v_mul_f32_e32 v33, 0x3db8aa3b, v33
	v_sub_f32_e32 v26, v26, v31
	v_mul_f32_e32 v27, 0x3db8aa3b, v27
	v_add_f32_e32 v32, v32, v65
	v_exp_f32_e32 v69, v33
	v_mul_f32_e32 v26, 0x3db8aa3b, v26
	v_exp_f32_e32 v71, v27
	v_sub_f32_e32 v27, v28, v31
	v_add_f32_e32 v32, v32, v66
	v_exp_f32_e32 v70, v26
	v_mul_f32_e32 v27, 0x3db8aa3b, v27
	v_add_f32_e32 v32, v32, v67
	v_exp_f32_e32 v72, v27
	v_sub_f32_e32 v27, v29, v31
	v_add_f32_e32 v32, v32, v68
	v_mul_f32_e32 v27, 0x3db8aa3b, v27
	v_add_f32_e32 v32, v32, v69
	v_exp_f32_e32 v73, v27
	v_add_f32_e32 v26, v32, v70
	v_add_f32_e32 v26, v26, v71
	v_add_f32_e32 v26, v26, v72
	v_add_f32_e32 v26, v26, v73
	ds_bpermute_b32 v1, v1, v26
	s_waitcnt lgkmcnt(0)
	v_add_f32_e32 v1, v26, v1
	ds_bpermute_b32 v26, v30, v1
	s_waitcnt lgkmcnt(0)
	v_add_f32_e32 v1, v1, v26
	v_div_scale_f32 v26, s[36:37], v1, v1, 1.0
	v_rcp_f32_e32 v27, v26
	s_nop 0
	v_fma_f32 v28, -v26, v27, 1.0
	v_fmac_f32_e32 v27, v28, v27
	v_div_scale_f32 v28, vcc, 1.0, v1, 1.0
	v_mul_f32_e32 v29, v28, v27
	v_fma_f32 v30, -v26, v29, v28
	v_fmac_f32_e32 v29, v30, v27
	v_fma_f32 v26, -v26, v29, v28
	v_div_fmas_f32 v26, v26, v27, v29
	v_div_fixup_f32 v1, v26, v1, 1.0
	v_mul_f32_e32 v2, v1, v2
	v_mul_f32_e32 v3, v1, v3
	v_cvt_pk_bf16_f32 v30, v2, v3
	v_mul_f32_e32 v2, v1, v4
	v_mul_f32_e32 v3, v1, v5
	v_cvt_pk_bf16_f32 v31, v2, v3
	v_mul_f32_e32 v2, v1, v18
	v_mul_f32_e32 v3, v1, v19
	v_cvt_pk_bf16_f32 v32, v2, v3
	v_mul_f32_e32 v2, v1, v20
	v_mul_f32_e32 v3, v1, v21
	v_cvt_pk_bf16_f32 v33, v2, v3
	v_mul_f32_e32 v2, v1, v6
	v_mul_f32_e32 v3, v1, v7
	v_cvt_pk_bf16_f32 v26, v2, v3
	v_mul_f32_e32 v2, v1, v8
	v_mul_f32_e32 v3, v1, v9
	v_cvt_pk_bf16_f32 v27, v2, v3
	v_mul_f32_e32 v2, v1, v22
	v_mul_f32_e32 v3, v1, v23
	v_cvt_pk_bf16_f32 v28, v2, v3
	v_mul_f32_e32 v2, v1, v24
	v_mul_f32_e32 v3, v1, v25
	v_cvt_pk_bf16_f32 v29, v2, v3
	v_mul_f32_e32 v2, v1, v10
	v_mul_f32_e32 v3, v1, v11
	v_cvt_pk_bf16_f32 v22, v2, v3
	v_mul_f32_e32 v2, v1, v12
	v_mul_f32_e32 v3, v1, v13
	v_cvt_pk_bf16_f32 v23, v2, v3
	v_mul_f32_e32 v2, v1, v34
	v_mul_f32_e32 v3, v1, v35
	v_lshl_add_u64 v[34:35], s[6:7], 0, v[96:97]
	v_lshlrev_b64 v[34:35], 11, v[34:35]
	v_lshl_add_u64 v[34:35], s[2:3], 0, v[34:35]
	v_lshl_add_u64 v[34:35], s[12:13], 1, v[34:35]
	v_lshl_add_u64 v[74:75], v[34:35], 0, v[100:101]
	v_add_co_u32_e32 v34, vcc, s19, v74
	global_load_dwordx4 v[86:89], v[74:75], off
	s_nop 0
	v_addc_co_u32_e32 v35, vcc, 0, v75, vcc
	global_load_dwordx4 v[90:93], v[34:35], off
	v_add_co_u32_e32 v34, vcc, s17, v74
	v_cvt_pk_bf16_f32 v24, v2, v3
	v_mul_f32_e32 v2, v1, v36
	s_nop 0
	v_addc_co_u32_e32 v35, vcc, 0, v75, vcc
	global_load_dwordx4 v[226:229], v[34:35], off
	v_add_co_u32_e32 v34, vcc, s18, v74
	v_mul_f32_e32 v3, v1, v37
	s_nop 0
	v_addc_co_u32_e32 v35, vcc, 0, v75, vcc
	global_load_dwordx4 v[78:81], v[34:35], off
	v_add_co_u32_e32 v34, vcc, s20, v74
	v_cvt_pk_bf16_f32 v25, v2, v3
	v_mul_f32_e32 v2, v1, v14
	s_nop 0
	v_addc_co_u32_e32 v35, vcc, 0, v75, vcc
	v_mul_f32_e32 v3, v1, v15
	global_load_dwordx4 v[82:85], v[34:35], off
	v_add_co_u32_e32 v34, vcc, s21, v74
	v_cvt_pk_bf16_f32 v18, v2, v3
	v_mul_f32_e32 v2, v1, v16
	v_mul_f32_e32 v3, v1, v17
	v_addc_co_u32_e32 v35, vcc, 0, v75, vcc
	v_cvt_pk_bf16_f32 v19, v2, v3
	v_mul_f32_e32 v2, v1, v38
	v_mul_f32_e32 v3, v1, v39
	v_add_co_u32_e32 v38, vcc, s22, v74
	v_cvt_pk_bf16_f32 v20, v2, v3
	v_mul_f32_e32 v2, v1, v40
	v_mul_f32_e32 v3, v1, v41
	v_addc_co_u32_e32 v39, vcc, 0, v75, vcc
	v_cvt_pk_bf16_f32 v21, v2, v3
	v_mul_f32_e32 v2, v1, v42
	v_mul_f32_e32 v3, v1, v43
	v_add_co_u32_e32 v42, vcc, s23, v74
	v_cvt_pk_bf16_f32 v14, v2, v3
	v_mul_f32_e32 v2, v1, v44
	v_mul_f32_e32 v3, v1, v45
	v_addc_co_u32_e32 v43, vcc, 0, v75, vcc
	v_cvt_pk_bf16_f32 v15, v2, v3
	v_mul_f32_e32 v2, v1, v46
	v_mul_f32_e32 v3, v1, v47
	v_add_co_u32_e32 v46, vcc, s24, v74
	v_cvt_pk_bf16_f32 v16, v2, v3
	v_mul_f32_e32 v2, v1, v48
	v_mul_f32_e32 v3, v1, v49
	v_addc_co_u32_e32 v47, vcc, 0, v75, vcc
	v_cvt_pk_bf16_f32 v17, v2, v3
	v_mul_f32_e32 v2, v1, v50
	v_mul_f32_e32 v3, v1, v51
	v_add_co_u32_e32 v50, vcc, s25, v74
	v_cvt_pk_bf16_f32 v10, v2, v3
	v_mul_f32_e32 v2, v1, v52
	v_mul_f32_e32 v3, v1, v53
	v_addc_co_u32_e32 v51, vcc, 0, v75, vcc
	v_cvt_pk_bf16_f32 v11, v2, v3
	v_mul_f32_e32 v2, v1, v54
	v_mul_f32_e32 v3, v1, v55
	v_add_co_u32_e32 v54, vcc, s26, v74
	v_cvt_pk_bf16_f32 v12, v2, v3
	v_mul_f32_e32 v2, v1, v56
	v_mul_f32_e32 v3, v1, v57
	v_addc_co_u32_e32 v55, vcc, 0, v75, vcc
	v_cvt_pk_bf16_f32 v13, v2, v3
	v_mul_f32_e32 v2, v1, v58
	v_mul_f32_e32 v3, v1, v59
	global_load_dwordx4 v[34:37], v[34:35], off
	v_add_co_u32_e32 v58, vcc, s27, v74
	v_cvt_pk_bf16_f32 v6, v2, v3
	v_mul_f32_e32 v2, v1, v60
	v_mul_f32_e32 v3, v1, v61
	global_load_dwordx4 v[38:41], v[38:39], off
	v_addc_co_u32_e32 v59, vcc, 0, v75, vcc
	v_cvt_pk_bf16_f32 v7, v2, v3
	v_mul_f32_e32 v2, v1, v62
	v_mul_f32_e32 v3, v1, v63
	global_load_dwordx4 v[42:45], v[42:43], off
	v_add_co_u32_e32 v62, vcc, s28, v74
	v_cvt_pk_bf16_f32 v8, v2, v3
	v_mul_f32_e32 v2, v1, v64
	v_mul_f32_e32 v3, v1, v65
	global_load_dwordx4 v[46:49], v[46:47], off
	v_addc_co_u32_e32 v63, vcc, 0, v75, vcc
	v_cvt_pk_bf16_f32 v9, v2, v3
	v_mul_f32_e32 v2, v1, v66
	v_mul_f32_e32 v3, v1, v67
	global_load_dwordx4 v[50:53], v[50:51], off
	v_add_co_u32_e32 v66, vcc, s29, v74
	v_cvt_pk_bf16_f32 v2, v2, v3
	v_mul_f32_e32 v3, v1, v68
	v_mul_f32_e32 v4, v1, v69
	global_load_dwordx4 v[54:57], v[54:55], off
	v_addc_co_u32_e32 v67, vcc, 0, v75, vcc
	v_cvt_pk_bf16_f32 v3, v3, v4
	v_mul_f32_e32 v4, v1, v70
	global_load_dwordx4 v[58:61], v[58:59], off
	v_add_co_u32_e32 v70, vcc, s30, v74
	v_mul_f32_e32 v5, v1, v71
	global_load_dwordx4 v[62:65], v[62:63], off
	v_addc_co_u32_e32 v71, vcc, 0, v75, vcc
	global_load_dwordx4 v[66:69], v[66:67], off
	v_add_co_u32_e32 v74, vcc, s31, v74
	v_cvt_pk_bf16_f32 v4, v4, v5
	v_mul_f32_e32 v5, v1, v72
	v_mul_f32_e32 v1, v1, v73
	global_load_dwordx4 v[70:73], v[70:71], off
	v_addc_co_u32_e32 v75, vcc, 0, v75, vcc
	global_load_dwordx4 v[74:77], v[74:75], off
	s_barrier
	s_waitcnt vmcnt(15)
	ds_write_b128 v114, v[86:89]
	s_waitcnt vmcnt(14)
	ds_write_b128 v114, v[90:93] offset:8192
	s_waitcnt vmcnt(13)
	ds_write_b128 v114, v[226:229] offset:16384
	s_waitcnt vmcnt(12)
	ds_write_b128 v114, v[78:81] offset:24576
	s_waitcnt vmcnt(11)
	ds_write_b128 v114, v[82:85] offset:32768
	s_waitcnt vmcnt(10)
	ds_write_b128 v114, v[34:37] offset:40960
	s_waitcnt vmcnt(9)
	ds_write_b128 v114, v[38:41] offset:49152
	s_waitcnt vmcnt(8)
	ds_write_b128 v114, v[42:45] offset:57344
	s_waitcnt vmcnt(7)
	ds_write_b128 v133, v[46:49]
	s_waitcnt vmcnt(6)
	ds_write_b128 v134, v[50:53]
	s_waitcnt vmcnt(5)
	ds_write_b128 v135, v[54:57]
	s_waitcnt vmcnt(4)
	ds_write_b128 v136, v[58:61]
	s_waitcnt vmcnt(3)
	ds_write_b128 v137, v[62:65]
	s_waitcnt vmcnt(2)
	ds_write_b128 v138, v[66:69]
	s_waitcnt vmcnt(1)
	ds_write_b128 v139, v[70:73]
	s_waitcnt vmcnt(0)
	ds_write_b128 v140, v[74:77]
	s_waitcnt lgkmcnt(0)
	s_barrier
	ds_read_b128 v[34:37], v141
	ds_read_b128 v[38:41], v141 offset:8192
	ds_read_b128 v[42:45], v141 offset:16384
	ds_read_b128 v[46:49], v141 offset:24576
	ds_read_b128 v[50:53], v141 offset:32768
	ds_read_b128 v[54:57], v141 offset:40960
	ds_read_b128 v[58:61], v141 offset:49152
	ds_read_b128 v[62:65], v141 offset:57344
	ds_read_b128 v[66:69], v142
	ds_read_b128 v[70:73], v143
	ds_read_b128 v[74:77], v144
	ds_read_b128 v[78:81], v145
	ds_read_b128 v[82:85], v146
	ds_read_b128 v[86:89], v147
	ds_read_b128 v[90:93], v148
	ds_read_b128 v[226:229], v149
	s_waitcnt lgkmcnt(14)
	v_mfma_f32_16x16x32_bf16 v[34:37], v[34:37], v[30:33], 0
	v_cvt_pk_bf16_f32 v5, v5, v1
	s_add_i32 s6, s34, s81
	v_mfma_f32_16x16x32_bf16 v[38:41], v[38:41], v[30:33], 0
	s_waitcnt lgkmcnt(13)
	v_mfma_f32_16x16x32_bf16 v[42:45], v[42:45], v[30:33], 0
	s_waitcnt lgkmcnt(12)
	v_mfma_f32_16x16x32_bf16 v[46:49], v[46:49], v[30:33], 0
	s_waitcnt lgkmcnt(11)
	v_mfma_f32_16x16x32_bf16 v[50:53], v[50:53], v[30:33], 0
	s_waitcnt lgkmcnt(10)
	v_mfma_f32_16x16x32_bf16 v[54:57], v[54:57], v[30:33], 0
	s_waitcnt lgkmcnt(9)
	v_mfma_f32_16x16x32_bf16 v[58:61], v[58:61], v[30:33], 0
	s_waitcnt lgkmcnt(8)
	v_mfma_f32_16x16x32_bf16 v[62:65], v[62:65], v[30:33], 0
	s_waitcnt lgkmcnt(7)
	v_mfma_f32_16x16x32_bf16 v[66:69], v[66:69], v[30:33], 0
	s_waitcnt lgkmcnt(6)
	v_mfma_f32_16x16x32_bf16 v[70:73], v[70:73], v[30:33], 0
	s_waitcnt lgkmcnt(5)
	v_mfma_f32_16x16x32_bf16 v[74:77], v[74:77], v[30:33], 0
	s_waitcnt lgkmcnt(4)
	v_mfma_f32_16x16x32_bf16 v[78:81], v[78:81], v[30:33], 0
	s_waitcnt lgkmcnt(3)
	v_mfma_f32_16x16x32_bf16 v[82:85], v[82:85], v[30:33], 0
	s_waitcnt lgkmcnt(2)
	v_mfma_f32_16x16x32_bf16 v[86:89], v[86:89], v[30:33], 0
	s_waitcnt lgkmcnt(1)
	v_mfma_f32_16x16x32_bf16 v[90:93], v[90:93], v[30:33], 0
	s_waitcnt lgkmcnt(0)
	v_mfma_f32_16x16x32_bf16 v[30:33], v[226:229], v[30:33], 0
	ds_read_b128 v[226:229], v150
	s_waitcnt lgkmcnt(0)
	v_mfma_f32_16x16x32_bf16 v[34:37], v[226:229], v[26:29], v[34:37]
	ds_read_b128 v[226:229], v150 offset:8192
	s_waitcnt lgkmcnt(0)
	v_mfma_f32_16x16x32_bf16 v[38:41], v[226:229], v[26:29], v[38:41]
	ds_read_b128 v[226:229], v150 offset:16384
	s_waitcnt lgkmcnt(0)
	v_mfma_f32_16x16x32_bf16 v[42:45], v[226:229], v[26:29], v[42:45]
	ds_read_b128 v[226:229], v150 offset:24576
	s_waitcnt lgkmcnt(0)
	v_mfma_f32_16x16x32_bf16 v[46:49], v[226:229], v[26:29], v[46:49]
	ds_read_b128 v[226:229], v150 offset:32768
	s_waitcnt lgkmcnt(0)
	v_mfma_f32_16x16x32_bf16 v[50:53], v[226:229], v[26:29], v[50:53]
	ds_read_b128 v[226:229], v150 offset:40960
	s_waitcnt lgkmcnt(0)
	v_mfma_f32_16x16x32_bf16 v[54:57], v[226:229], v[26:29], v[54:57]
	ds_read_b128 v[226:229], v150 offset:49152
	s_waitcnt lgkmcnt(0)
	v_mfma_f32_16x16x32_bf16 v[58:61], v[226:229], v[26:29], v[58:61]
	ds_read_b128 v[226:229], v150 offset:57344
	s_waitcnt lgkmcnt(0)
	v_mfma_f32_16x16x32_bf16 v[62:65], v[226:229], v[26:29], v[62:65]
	ds_read_b128 v[226:229], v151
	s_waitcnt lgkmcnt(0)
	v_mfma_f32_16x16x32_bf16 v[66:69], v[226:229], v[26:29], v[66:69]
	ds_read_b128 v[226:229], v152
	s_waitcnt lgkmcnt(0)
	v_mfma_f32_16x16x32_bf16 v[70:73], v[226:229], v[26:29], v[70:73]
	ds_read_b128 v[226:229], v153
	s_waitcnt lgkmcnt(0)
	v_mfma_f32_16x16x32_bf16 v[74:77], v[226:229], v[26:29], v[74:77]
	ds_read_b128 v[226:229], v154
	s_waitcnt lgkmcnt(0)
	v_mfma_f32_16x16x32_bf16 v[78:81], v[226:229], v[26:29], v[78:81]
	ds_read_b128 v[226:229], v155
	s_waitcnt lgkmcnt(0)
	v_mfma_f32_16x16x32_bf16 v[82:85], v[226:229], v[26:29], v[82:85]
	ds_read_b128 v[226:229], v156
	s_waitcnt lgkmcnt(0)
	v_mfma_f32_16x16x32_bf16 v[86:89], v[226:229], v[26:29], v[86:89]
	ds_read_b128 v[226:229], v157
	s_waitcnt lgkmcnt(0)
	v_mfma_f32_16x16x32_bf16 v[90:93], v[226:229], v[26:29], v[90:93]
	ds_read_b128 v[226:229], v158
	s_waitcnt lgkmcnt(0)
	v_mfma_f32_16x16x32_bf16 v[26:29], v[226:229], v[26:29], v[30:33]
	s_nop 2
	ds_read_b128 v[30:33], v159
	s_waitcnt lgkmcnt(0)
	v_mfma_f32_16x16x32_bf16 v[30:33], v[30:33], v[22:25], v[34:37]
	s_nop 2
	ds_read_b128 v[34:37], v159 offset:8192
	s_waitcnt lgkmcnt(0)
	v_mfma_f32_16x16x32_bf16 v[34:37], v[34:37], v[22:25], v[38:41]
	s_nop 2
	ds_read_b128 v[38:41], v159 offset:16384
	s_waitcnt lgkmcnt(0)
	v_mfma_f32_16x16x32_bf16 v[38:41], v[38:41], v[22:25], v[42:45]
	s_nop 2
	ds_read_b128 v[42:45], v159 offset:24576
	s_waitcnt lgkmcnt(0)
	v_mfma_f32_16x16x32_bf16 v[42:45], v[42:45], v[22:25], v[46:49]
	s_nop 2
	ds_read_b128 v[46:49], v159 offset:32768
	s_waitcnt lgkmcnt(0)
	v_mfma_f32_16x16x32_bf16 v[46:49], v[46:49], v[22:25], v[50:53]
	s_nop 2
	ds_read_b128 v[50:53], v159 offset:40960
	s_waitcnt lgkmcnt(0)
	v_mfma_f32_16x16x32_bf16 v[50:53], v[50:53], v[22:25], v[54:57]
	s_nop 2
	ds_read_b128 v[54:57], v159 offset:49152
	s_waitcnt lgkmcnt(0)
	v_mfma_f32_16x16x32_bf16 v[54:57], v[54:57], v[22:25], v[58:61]
	s_nop 2
	ds_read_b128 v[58:61], v159 offset:57344
	s_waitcnt lgkmcnt(0)
	v_mfma_f32_16x16x32_bf16 v[58:61], v[58:61], v[22:25], v[62:65]
	s_nop 2
	ds_read_b128 v[62:65], v160
	s_waitcnt lgkmcnt(0)
	v_mfma_f32_16x16x32_bf16 v[62:65], v[62:65], v[22:25], v[66:69]
	s_nop 2
	ds_read_b128 v[66:69], v161
	s_waitcnt lgkmcnt(0)
	v_mfma_f32_16x16x32_bf16 v[66:69], v[66:69], v[22:25], v[70:73]
	s_nop 2
	ds_read_b128 v[70:73], v162
	s_waitcnt lgkmcnt(0)
	v_mfma_f32_16x16x32_bf16 v[70:73], v[70:73], v[22:25], v[74:77]
	s_nop 2
	ds_read_b128 v[74:77], v163
	s_waitcnt lgkmcnt(0)
	v_mfma_f32_16x16x32_bf16 v[74:77], v[74:77], v[22:25], v[78:81]
	s_nop 2
	ds_read_b128 v[78:81], v164
	s_waitcnt lgkmcnt(0)
	v_mfma_f32_16x16x32_bf16 v[78:81], v[78:81], v[22:25], v[82:85]
	s_nop 2
	ds_read_b128 v[82:85], v165
	s_waitcnt lgkmcnt(0)
	v_mfma_f32_16x16x32_bf16 v[82:85], v[82:85], v[22:25], v[86:89]
	s_nop 2
	ds_read_b128 v[86:89], v166
	s_waitcnt lgkmcnt(0)
	v_mfma_f32_16x16x32_bf16 v[86:89], v[86:89], v[22:25], v[90:93]
	s_nop 2
	ds_read_b128 v[90:93], v167
	s_waitcnt lgkmcnt(0)
	v_mfma_f32_16x16x32_bf16 v[22:25], v[90:93], v[22:25], v[26:29]
	s_nop 2
	ds_read_b128 v[26:29], v168
	s_waitcnt lgkmcnt(0)
	v_mfma_f32_16x16x32_bf16 v[26:29], v[26:29], v[18:21], v[30:33]
	s_nop 2
	ds_read_b128 v[30:33], v168 offset:8192
	s_waitcnt lgkmcnt(0)
	v_mfma_f32_16x16x32_bf16 v[30:33], v[30:33], v[18:21], v[34:37]
	s_nop 2
	ds_read_b128 v[34:37], v168 offset:16384
	s_waitcnt lgkmcnt(0)
	v_mfma_f32_16x16x32_bf16 v[34:37], v[34:37], v[18:21], v[38:41]
	s_nop 2
	ds_read_b128 v[38:41], v168 offset:24576
	s_waitcnt lgkmcnt(0)
	v_mfma_f32_16x16x32_bf16 v[38:41], v[38:41], v[18:21], v[42:45]
	s_nop 2
	ds_read_b128 v[42:45], v168 offset:32768
	s_waitcnt lgkmcnt(0)
	v_mfma_f32_16x16x32_bf16 v[42:45], v[42:45], v[18:21], v[46:49]
	s_nop 2
	ds_read_b128 v[46:49], v168 offset:40960
	s_waitcnt lgkmcnt(0)
	v_mfma_f32_16x16x32_bf16 v[46:49], v[46:49], v[18:21], v[50:53]
	s_nop 2
	ds_read_b128 v[50:53], v168 offset:49152
	s_waitcnt lgkmcnt(0)
	v_mfma_f32_16x16x32_bf16 v[50:53], v[50:53], v[18:21], v[54:57]
	s_nop 2
	ds_read_b128 v[54:57], v168 offset:57344
	s_waitcnt lgkmcnt(0)
	v_mfma_f32_16x16x32_bf16 v[54:57], v[54:57], v[18:21], v[58:61]
	s_nop 2
	ds_read_b128 v[58:61], v169
	s_waitcnt lgkmcnt(0)
	v_mfma_f32_16x16x32_bf16 v[58:61], v[58:61], v[18:21], v[62:65]
	s_nop 2
	ds_read_b128 v[62:65], v170
	s_waitcnt lgkmcnt(0)
	v_mfma_f32_16x16x32_bf16 v[62:65], v[62:65], v[18:21], v[66:69]
	s_nop 2
	ds_read_b128 v[66:69], v171
	s_waitcnt lgkmcnt(0)
	v_mfma_f32_16x16x32_bf16 v[66:69], v[66:69], v[18:21], v[70:73]
	s_nop 2
	ds_read_b128 v[70:73], v172
	s_waitcnt lgkmcnt(0)
	v_mfma_f32_16x16x32_bf16 v[70:73], v[70:73], v[18:21], v[74:77]
	s_nop 2
	ds_read_b128 v[74:77], v173
	s_waitcnt lgkmcnt(0)
	v_mfma_f32_16x16x32_bf16 v[74:77], v[74:77], v[18:21], v[78:81]
	s_nop 2
	ds_read_b128 v[78:81], v174
	s_waitcnt lgkmcnt(0)
	v_mfma_f32_16x16x32_bf16 v[78:81], v[78:81], v[18:21], v[82:85]
	s_nop 2
	ds_read_b128 v[82:85], v175
	s_waitcnt lgkmcnt(0)
	v_mfma_f32_16x16x32_bf16 v[82:85], v[82:85], v[18:21], v[86:89]
	s_nop 2
	ds_read_b128 v[86:89], v176
	s_waitcnt lgkmcnt(0)
	v_mfma_f32_16x16x32_bf16 v[18:21], v[86:89], v[18:21], v[22:25]
	s_nop 2
	ds_read_b128 v[22:25], v177
	s_waitcnt lgkmcnt(0)
	v_mfma_f32_16x16x32_bf16 v[22:25], v[22:25], v[14:17], v[26:29]
	s_nop 2
	ds_read_b128 v[26:29], v177 offset:8192
	s_waitcnt lgkmcnt(0)
	v_mfma_f32_16x16x32_bf16 v[26:29], v[26:29], v[14:17], v[30:33]
	s_nop 2
	ds_read_b128 v[30:33], v177 offset:16384
	s_waitcnt lgkmcnt(0)
	v_mfma_f32_16x16x32_bf16 v[30:33], v[30:33], v[14:17], v[34:37]
	s_nop 2
	ds_read_b128 v[34:37], v177 offset:24576
	s_waitcnt lgkmcnt(0)
	v_mfma_f32_16x16x32_bf16 v[34:37], v[34:37], v[14:17], v[38:41]
	s_nop 2
	ds_read_b128 v[38:41], v177 offset:32768
	s_waitcnt lgkmcnt(0)
	v_mfma_f32_16x16x32_bf16 v[38:41], v[38:41], v[14:17], v[42:45]
	s_nop 2
	ds_read_b128 v[42:45], v177 offset:40960
	s_waitcnt lgkmcnt(0)
	v_mfma_f32_16x16x32_bf16 v[42:45], v[42:45], v[14:17], v[46:49]
	s_nop 2
	ds_read_b128 v[46:49], v177 offset:49152
	s_waitcnt lgkmcnt(0)
	v_mfma_f32_16x16x32_bf16 v[46:49], v[46:49], v[14:17], v[50:53]
	s_nop 2
	ds_read_b128 v[50:53], v177 offset:57344
	s_waitcnt lgkmcnt(0)
	v_mfma_f32_16x16x32_bf16 v[50:53], v[50:53], v[14:17], v[54:57]
	s_nop 2
	ds_read_b128 v[54:57], v178
	s_waitcnt lgkmcnt(0)
	v_mfma_f32_16x16x32_bf16 v[54:57], v[54:57], v[14:17], v[58:61]
	s_nop 2
	ds_read_b128 v[58:61], v179
	s_waitcnt lgkmcnt(0)
	v_mfma_f32_16x16x32_bf16 v[58:61], v[58:61], v[14:17], v[62:65]
	s_nop 2
	ds_read_b128 v[62:65], v180
	s_waitcnt lgkmcnt(0)
	v_mfma_f32_16x16x32_bf16 v[62:65], v[62:65], v[14:17], v[66:69]
	s_nop 2
	ds_read_b128 v[66:69], v181
	s_waitcnt lgkmcnt(0)
	v_mfma_f32_16x16x32_bf16 v[66:69], v[66:69], v[14:17], v[70:73]
	s_nop 2
	ds_read_b128 v[70:73], v182
	s_waitcnt lgkmcnt(0)
	v_mfma_f32_16x16x32_bf16 v[70:73], v[70:73], v[14:17], v[74:77]
	s_nop 2
	ds_read_b128 v[74:77], v183
	s_waitcnt lgkmcnt(0)
	v_mfma_f32_16x16x32_bf16 v[74:77], v[74:77], v[14:17], v[78:81]
	s_nop 2
	ds_read_b128 v[78:81], v184
	s_waitcnt lgkmcnt(0)
	v_mfma_f32_16x16x32_bf16 v[78:81], v[78:81], v[14:17], v[82:85]
	s_nop 2
	ds_read_b128 v[82:85], v185
	s_waitcnt lgkmcnt(0)
	v_mfma_f32_16x16x32_bf16 v[14:17], v[82:85], v[14:17], v[18:21]
	s_nop 2
	ds_read_b128 v[18:21], v186
	s_waitcnt lgkmcnt(0)
	v_mfma_f32_16x16x32_bf16 v[18:21], v[18:21], v[10:13], v[22:25]
	s_nop 2
	ds_read_b128 v[22:25], v186 offset:8192
	s_waitcnt lgkmcnt(0)
	v_mfma_f32_16x16x32_bf16 v[22:25], v[22:25], v[10:13], v[26:29]
	s_nop 2
	ds_read_b128 v[26:29], v186 offset:16384
	s_waitcnt lgkmcnt(0)
	v_mfma_f32_16x16x32_bf16 v[26:29], v[26:29], v[10:13], v[30:33]
	s_nop 2
	ds_read_b128 v[30:33], v186 offset:24576
	s_waitcnt lgkmcnt(0)
	v_mfma_f32_16x16x32_bf16 v[30:33], v[30:33], v[10:13], v[34:37]
	s_nop 2
	ds_read_b128 v[34:37], v186 offset:32768
	s_waitcnt lgkmcnt(0)
	v_mfma_f32_16x16x32_bf16 v[34:37], v[34:37], v[10:13], v[38:41]
	s_nop 2
	ds_read_b128 v[38:41], v186 offset:40960
	s_waitcnt lgkmcnt(0)
	v_mfma_f32_16x16x32_bf16 v[38:41], v[38:41], v[10:13], v[42:45]
	s_nop 2
	ds_read_b128 v[42:45], v186 offset:49152
	s_waitcnt lgkmcnt(0)
	v_mfma_f32_16x16x32_bf16 v[42:45], v[42:45], v[10:13], v[46:49]
	s_nop 2
	ds_read_b128 v[46:49], v186 offset:57344
	s_waitcnt lgkmcnt(0)
	v_mfma_f32_16x16x32_bf16 v[46:49], v[46:49], v[10:13], v[50:53]
	s_nop 2
	ds_read_b128 v[50:53], v187
	s_waitcnt lgkmcnt(0)
	v_mfma_f32_16x16x32_bf16 v[50:53], v[50:53], v[10:13], v[54:57]
	s_nop 2
	ds_read_b128 v[54:57], v188
	s_waitcnt lgkmcnt(0)
	v_mfma_f32_16x16x32_bf16 v[54:57], v[54:57], v[10:13], v[58:61]
	s_nop 2
	ds_read_b128 v[58:61], v189
	s_waitcnt lgkmcnt(0)
	v_mfma_f32_16x16x32_bf16 v[58:61], v[58:61], v[10:13], v[62:65]
	s_nop 2
	ds_read_b128 v[62:65], v190
	s_waitcnt lgkmcnt(0)
	v_mfma_f32_16x16x32_bf16 v[62:65], v[62:65], v[10:13], v[66:69]
	s_nop 2
	ds_read_b128 v[66:69], v191
	s_waitcnt lgkmcnt(0)
	v_mfma_f32_16x16x32_bf16 v[66:69], v[66:69], v[10:13], v[70:73]
	s_nop 2
	ds_read_b128 v[70:73], v192
	s_waitcnt lgkmcnt(0)
	v_mfma_f32_16x16x32_bf16 v[70:73], v[70:73], v[10:13], v[74:77]
	s_nop 2
	ds_read_b128 v[74:77], v193
	s_waitcnt lgkmcnt(0)
	v_mfma_f32_16x16x32_bf16 v[74:77], v[74:77], v[10:13], v[78:81]
	s_nop 2
	ds_read_b128 v[78:81], v194
	s_waitcnt lgkmcnt(0)
	v_mfma_f32_16x16x32_bf16 v[10:13], v[78:81], v[10:13], v[14:17]
	s_nop 2
	ds_read_b128 v[14:17], v195
	s_waitcnt lgkmcnt(0)
	v_mfma_f32_16x16x32_bf16 v[14:17], v[14:17], v[6:9], v[18:21]
	s_nop 2
	ds_read_b128 v[18:21], v195 offset:8192
	s_waitcnt lgkmcnt(0)
	v_mfma_f32_16x16x32_bf16 v[18:21], v[18:21], v[6:9], v[22:25]
	s_nop 2
	ds_read_b128 v[22:25], v195 offset:16384
	s_waitcnt lgkmcnt(0)
	v_mfma_f32_16x16x32_bf16 v[22:25], v[22:25], v[6:9], v[26:29]
	s_nop 2
	ds_read_b128 v[26:29], v195 offset:24576
	s_waitcnt lgkmcnt(0)
	v_mfma_f32_16x16x32_bf16 v[26:29], v[26:29], v[6:9], v[30:33]
	s_nop 2
	ds_read_b128 v[30:33], v195 offset:32768
	s_waitcnt lgkmcnt(0)
	v_mfma_f32_16x16x32_bf16 v[30:33], v[30:33], v[6:9], v[34:37]
	s_nop 2
	ds_read_b128 v[34:37], v195 offset:40960
	s_waitcnt lgkmcnt(0)
	v_mfma_f32_16x16x32_bf16 v[34:37], v[34:37], v[6:9], v[38:41]
	s_nop 2
	ds_read_b128 v[38:41], v195 offset:49152
	s_waitcnt lgkmcnt(0)
	v_mfma_f32_16x16x32_bf16 v[38:41], v[38:41], v[6:9], v[42:45]
	s_nop 2
	ds_read_b128 v[42:45], v195 offset:57344
	s_waitcnt lgkmcnt(0)
	v_mfma_f32_16x16x32_bf16 v[42:45], v[42:45], v[6:9], v[46:49]
	s_nop 2
	ds_read_b128 v[46:49], v196
	s_waitcnt lgkmcnt(0)
	v_mfma_f32_16x16x32_bf16 v[46:49], v[46:49], v[6:9], v[50:53]
	s_nop 2
	ds_read_b128 v[50:53], v197
	s_waitcnt lgkmcnt(0)
	v_mfma_f32_16x16x32_bf16 v[50:53], v[50:53], v[6:9], v[54:57]
	s_nop 2
	ds_read_b128 v[54:57], v198
	s_waitcnt lgkmcnt(0)
	v_mfma_f32_16x16x32_bf16 v[54:57], v[54:57], v[6:9], v[58:61]
	s_nop 2
	ds_read_b128 v[58:61], v199
	s_waitcnt lgkmcnt(0)
	v_mfma_f32_16x16x32_bf16 v[58:61], v[58:61], v[6:9], v[62:65]
	s_nop 2
	ds_read_b128 v[62:65], v200
	s_waitcnt lgkmcnt(0)
	v_mfma_f32_16x16x32_bf16 v[62:65], v[62:65], v[6:9], v[66:69]
	s_nop 2
	ds_read_b128 v[66:69], v201
	s_waitcnt lgkmcnt(0)
	v_mfma_f32_16x16x32_bf16 v[66:69], v[66:69], v[6:9], v[70:73]
	s_nop 2
	ds_read_b128 v[70:73], v202
	s_waitcnt lgkmcnt(0)
	v_mfma_f32_16x16x32_bf16 v[70:73], v[70:73], v[6:9], v[74:77]
	s_nop 2
	ds_read_b128 v[74:77], v203
	s_waitcnt lgkmcnt(0)
	v_mfma_f32_16x16x32_bf16 v[6:9], v[74:77], v[6:9], v[10:13]
	s_nop 2
	ds_read_b128 v[10:13], v204
	s_waitcnt lgkmcnt(0)
	v_mfma_f32_16x16x32_bf16 v[10:13], v[10:13], v[2:5], v[14:17]
	s_nop 2
	ds_read_b128 v[14:17], v204 offset:8192
	s_waitcnt lgkmcnt(0)
	v_mfma_f32_16x16x32_bf16 v[14:17], v[14:17], v[2:5], v[18:21]
	s_nop 2
	ds_read_b128 v[18:21], v204 offset:16384
	s_waitcnt lgkmcnt(0)
	v_mfma_f32_16x16x32_bf16 v[18:21], v[18:21], v[2:5], v[22:25]
	s_nop 2
	ds_read_b128 v[22:25], v204 offset:24576
	s_waitcnt lgkmcnt(0)
	v_mfma_f32_16x16x32_bf16 v[22:25], v[22:25], v[2:5], v[26:29]
	s_nop 2
	ds_read_b128 v[26:29], v204 offset:32768
	s_waitcnt lgkmcnt(0)
	v_mfma_f32_16x16x32_bf16 v[26:29], v[26:29], v[2:5], v[30:33]
	s_nop 2
	ds_read_b128 v[30:33], v204 offset:40960
	s_waitcnt lgkmcnt(0)
	v_mfma_f32_16x16x32_bf16 v[30:33], v[30:33], v[2:5], v[34:37]
	s_nop 2
	ds_read_b128 v[34:37], v204 offset:49152
	s_waitcnt lgkmcnt(0)
	v_mfma_f32_16x16x32_bf16 v[34:37], v[34:37], v[2:5], v[38:41]
	s_nop 2
	ds_read_b128 v[38:41], v204 offset:57344
	s_waitcnt lgkmcnt(0)
	v_mfma_f32_16x16x32_bf16 v[38:41], v[38:41], v[2:5], v[42:45]
	s_nop 2
	ds_read_b128 v[42:45], v205
	s_waitcnt lgkmcnt(0)
	v_mfma_f32_16x16x32_bf16 v[42:45], v[42:45], v[2:5], v[46:49]
	s_nop 2
	ds_read_b128 v[46:49], v206
	s_waitcnt lgkmcnt(0)
	v_mfma_f32_16x16x32_bf16 v[46:49], v[46:49], v[2:5], v[50:53]
	s_nop 2
	ds_read_b128 v[50:53], v207
	s_waitcnt lgkmcnt(0)
	v_mfma_f32_16x16x32_bf16 v[50:53], v[50:53], v[2:5], v[54:57]
	s_nop 2
	ds_read_b128 v[54:57], v208
	s_waitcnt lgkmcnt(0)
	v_mfma_f32_16x16x32_bf16 v[54:57], v[54:57], v[2:5], v[58:61]
	s_nop 2
	ds_read_b128 v[58:61], v209
	s_waitcnt lgkmcnt(0)
	v_mfma_f32_16x16x32_bf16 v[58:61], v[58:61], v[2:5], v[62:65]
	s_nop 2
	ds_read_b128 v[62:65], v210
	s_waitcnt lgkmcnt(0)
	v_mfma_f32_16x16x32_bf16 v[62:65], v[62:65], v[2:5], v[66:69]
	s_nop 2
	ds_read_b128 v[66:69], v211
	s_waitcnt lgkmcnt(0)
	v_mfma_f32_16x16x32_bf16 v[66:69], v[66:69], v[2:5], v[70:73]
	s_nop 2
	ds_read_b128 v[70:73], v212
	s_waitcnt lgkmcnt(0)
	v_mfma_f32_16x16x32_bf16 v[2:5], v[70:73], v[2:5], v[6:9]
	s_nop 2
	v_lshl_add_u64 v[6:7], s[4:5], 0, v[112:113]
	v_lshl_add_u64 v[70:71], v[6:7], 0, s[10:11]
	v_cvt_pk_bf16_f32 v6, v10, v11
	v_cvt_pk_bf16_f32 v7, v12, v13
	v_cvt_pk_bf16_f32 v8, v14, v15
	v_cvt_pk_bf16_f32 v9, v16, v17
	v_cvt_pk_bf16_f32 v10, v18, v19
	v_cvt_pk_bf16_f32 v11, v20, v21
	v_cvt_pk_bf16_f32 v12, v22, v23
	v_cvt_pk_bf16_f32 v13, v24, v25
	v_lshl_add_u64 v[14:15], v[70:71], 0, v[104:105]
	v_permlane32_swap_b32_e32 v6, v10
	v_permlane32_swap_b32_e32 v8, v12
	v_permlane32_swap_b32_e32 v7, v11
	v_permlane32_swap_b32_e32 v9, v13
	v_permlane16_swap_b32_e32 v6, v8
	v_permlane16_swap_b32_e32 v10, v12
	v_permlane16_swap_b32_e32 v7, v9
	v_permlane16_swap_b32_e32 v11, v13
	global_store_dwordx4 v[14:15], v[6:9], off
	global_store_dwordx4 v[14:15], v[10:13], off offset:16
	v_lshl_add_u64 v[14:15], v[70:71], 0, v[106:107]
	v_cvt_pk_bf16_f32 v6, v26, v27
	v_cvt_pk_bf16_f32 v7, v28, v29
	v_cvt_pk_bf16_f32 v8, v30, v31
	v_cvt_pk_bf16_f32 v9, v32, v33
	s_nop 0
	v_cvt_pk_bf16_f32 v10, v34, v35
	v_cvt_pk_bf16_f32 v11, v36, v37
	v_cvt_pk_bf16_f32 v12, v38, v39
	v_cvt_pk_bf16_f32 v13, v40, v41
	s_nop 0
	v_permlane32_swap_b32_e32 v6, v10
	v_permlane32_swap_b32_e32 v8, v12
	v_permlane32_swap_b32_e32 v7, v11
	v_permlane32_swap_b32_e32 v9, v13
	v_permlane16_swap_b32_e32 v6, v8
	v_permlane16_swap_b32_e32 v10, v12
	v_permlane16_swap_b32_e32 v7, v9
	v_permlane16_swap_b32_e32 v11, v13
	global_store_dwordx4 v[14:15], v[6:9], off
	global_store_dwordx4 v[14:15], v[10:13], off offset:16
	v_lshl_add_u64 v[14:15], v[70:71], 0, v[108:109]
	v_cvt_pk_bf16_f32 v6, v42, v43
	v_cvt_pk_bf16_f32 v7, v44, v45
	v_cvt_pk_bf16_f32 v8, v46, v47
	v_cvt_pk_bf16_f32 v9, v48, v49
	s_nop 0
	v_cvt_pk_bf16_f32 v10, v50, v51
	v_cvt_pk_bf16_f32 v11, v52, v53
	v_cvt_pk_bf16_f32 v12, v54, v55
	v_cvt_pk_bf16_f32 v13, v56, v57
	s_nop 0
	v_permlane32_swap_b32_e32 v6, v10
	v_permlane32_swap_b32_e32 v8, v12
	v_permlane32_swap_b32_e32 v7, v11
	v_permlane32_swap_b32_e32 v9, v13
	v_permlane16_swap_b32_e32 v6, v8
	v_permlane16_swap_b32_e32 v10, v12
	v_permlane16_swap_b32_e32 v7, v9
	v_permlane16_swap_b32_e32 v11, v13
	global_store_dwordx4 v[14:15], v[6:9], off
	global_store_dwordx4 v[14:15], v[10:13], off offset:16
	s_nop 0
	v_cvt_pk_bf16_f32 v6, v58, v59
	v_cvt_pk_bf16_f32 v7, v60, v61
	v_cvt_pk_bf16_f32 v8, v62, v63
	v_cvt_pk_bf16_f32 v9, v64, v65
	s_nop 0
	v_cvt_pk_bf16_f32 v10, v66, v67
	v_cvt_pk_bf16_f32 v11, v68, v69
	v_cvt_pk_bf16_f32 v12, v2, v3
	v_cvt_pk_bf16_f32 v13, v4, v5
	v_lshl_add_u64 v[2:3], v[70:71], 0, v[110:111]
	v_permlane32_swap_b32_e32 v6, v10
	v_permlane32_swap_b32_e32 v8, v12
	v_permlane32_swap_b32_e32 v7, v11
	v_permlane32_swap_b32_e32 v9, v13
	v_permlane16_swap_b32_e32 v6, v8
	s_nop 0
	v_permlane16_swap_b32_e32 v7, v9
	v_permlane16_swap_b32_e32 v10, v12
	v_permlane16_swap_b32_e32 v11, v13
	global_store_dwordx4 v[2:3], v[6:9], off
	global_store_dwordx4 v[2:3], v[10:13], off offset:16
	s_mov_b32 s34, s6
	s_cbranch_execz .LBB0_655
